# v4 + queue claim-ahead v2: t-queue claim at t_unit start, attention claim at unit epilogue start, no store drain at the claim barrier
# speedup vs baseline: 1.0056x; 1.0056x over previous
.LBB0_876:
	s_mov_b64 s[24:25], -1
	s_and_b64 vcc, exec, s[10:11]
	s_mov_b64 s[8:9], -1
	s_cbranch_vccnz .LBB0_875
	v_cmp_le_f32_e32 vcc, 1.0, v1
	s_or_b64 s[2:3], s[4:5], vcc
	s_and_b64 vcc, exec, s[2:3]
	s_cbranch_vccz .LBB0_874
	s_cmp_lg_u32 s99, 0
	s_cbranch_scc1 .Ltp_use
	s_waitcnt vmcnt(0)
	s_barrier
	s_and_saveexec_b64 s[8:9], s[0:1]
	s_cbranch_execz .LBB0_882
	s_mov_b64 s[12:13], exec
	v_mbcnt_lo_u32_b32 v2, s12, 0
	v_mbcnt_hi_u32_b32 v2, s13, v2
	v_cmp_eq_u32_e32 vcc, 0, v2
	s_and_saveexec_b64 s[10:11], vcc
	s_cbranch_execz .LBB0_881
	s_bcnt1_i32_b64 s2, s[12:13]
	v_mov_b32_e32 v4, s2
	global_atomic_add v4, v3, v4, s[28:29] sc0

.Ltp_join:
	v_readfirstlane_b32 s2, v4
	s_nop 1
	v_add_u32_e32 v2, s2, v2
	ds_write_b32 v237, v2
.LBB0_882:
	s_or_b64 exec, exec, s[8:9]
	s_waitcnt lgkmcnt(0)
	s_barrier
	ds_read_b32 v2, v237
	s_waitcnt lgkmcnt(0)
	v_readfirstlane_b32 s2, v2
	s_cmpk_gt_i32 s2, 0x47f
	s_cselect_b64 s[8:9], -1, 0
	s_and_b64 vcc, exec, s[8:9]
	s_cbranch_vccnz .LBB0_888
	s_and_saveexec_b64 s[100:101], s[0:1]
	s_cbranch_execz .Ltp_skip
	v_mov_b32_e32 v252, 0
	v_mov_b32_e32 v253, 1
	s_nop 0
	global_atomic_add v250, v252, v253, s[28:29] sc0
.Ltp_skip:
	s_or_b64 exec, exec, s[100:101]
	s_mov_b32 s99, 1
	s_mul_hi_i32 s3, s2, 0x71c71c72
	s_lshr_b32 s10, s3, 31
	s_ashr_i32 s3, s3, 4
	s_add_i32 s12, s3, s10
	s_mul_i32 s3, s12, 36
	s_sub_i32 s2, s2, s3
	s_mov_b64 s[14:15], s[44:45]
	v_mov_b32_e32 v4, v0
	s_add_i32 s3, s2, 4
	s_load_dwordx2 s[10:11], s[14:15], 0xd8
	s_cmp_lt_i32 s2, 32
	s_cselect_b32 s3, s2, s3
	v_readfirstlane_b32 s2, v4
	s_ashr_i32 s2, s2, 6
	v_lshlrev_b32_e32 v2, 1, v4
	v_lshlrev_b32_e32 v4, 2, v4
	s_cmp_gt_i32 s3, 31
	v_and_b32_e32 v2, 0x70, v2
	v_and_b32_e32 v134, 28, v4
	s_mov_b64 s[16:17], -1
	s_cbranch_scc0 .LBB0_885
	s_lshl_b32 s13, s3, 6
	s_add_i32 s13, s13, 0x7ffff800
	s_load_dwordx2 s[16:17], s[14:15], 0xc8
	s_and_b32 s79, s13, 0x7fffff80
	s_lshl_b32 s13, s3, 10
	s_and_b32 s13, s13, 0x400
	s_lshl_b32 s18, s2, 7
	s_add_i32 s18, s18, s13
	s_ashr_i32 s13, s12, 31
	s_lshl_b64 s[24:25], s[12:13], 23
	v_lshlrev_b32_e32 v135, 11, v2
	s_waitcnt lgkmcnt(0)
	s_add_u32 s24, s16, s24
	v_add_u32_e32 v4, s18, v135
	s_addc_u32 s19, s17, s25
	s_lshl_b64 s[16:17], s[12:13], 21
	v_or_b32_e32 v4, v4, v134
	s_lshl_b32 s13, s79, 13
	s_and_b32 s25, s19, 0xffff
	v_lshlrev_b32_e32 v4, 2, v4
	s_or_b32 s19, s13, 0x2000
	buffer_load_dwordx4 v[68:71], v4, s[24:27], s13 offen nt
	buffer_load_dwordx4 v[88:91], v4, s[24:27], s19 offen nt
	s_or_b32 s40, s13, 0x8000
	s_or_b32 s41, s13, 0xa000
	buffer_load_dwordx4 v[104:107], v4, s[24:27], s40 offen nt
	buffer_load_dwordx4 v[116:119], v4, s[24:27], s41 offen nt
	s_or_b32 s46, s13, 0x10000
	s_or_b32 s47, s13, 0x12000
	buffer_load_dwordx4 v[72:75], v4, s[24:27], s46 offen nt
	buffer_load_dwordx4 v[80:83], v4, s[24:27], s47 offen nt
	s_or_b32 s74, s13, 0x18000
	s_or_b32 s75, s13, 0x1a000
	buffer_load_dwordx4 v[76:79], v4, s[24:27], s74 offen nt
	buffer_load_dwordx4 v[96:99], v4, s[24:27], s75 offen nt
	s_or_b32 s22, s13, 0x4000
	s_or_b32 s33, s13, 0x6000
	s_or_b32 s50, s13, 0x14000
	s_or_b32 s51, s13, 0x16000
	buffer_load_dwordx4 v[100:103], v4, s[24:27], s22 offen nt
	buffer_load_dwordx4 v[112:115], v4, s[24:27], s33 offen nt
	s_or_b32 s42, s13, 0xc000
	s_or_b32 s43, s13, 0xe000
	buffer_load_dwordx4 v[84:87], v4, s[24:27], s50 offen nt
	buffer_load_dwordx4 v[92:95], v4, s[24:27], s51 offen nt
	s_or_b32 s76, s13, 0x1c000
	s_or_b32 s77, s13, 0x1e000
	buffer_load_dwordx4 v[124:127], v4, s[24:27], s42 offen nt
	buffer_load_dwordx4 v[128:131], v4, s[24:27], s43 offen nt
	buffer_load_dwordx4 v[108:111], v4, s[24:27], s76 offen nt
	buffer_load_dwordx4 v[120:123], v4, s[24:27], s77 offen nt
	s_or_b32 s78, s18, 32
	v_add_u32_e32 v4, s78, v135
	v_or_b32_e32 v4, v4, v134
	v_lshlrev_b32_e32 v16, 2, v4
	buffer_load_dwordx4 v[52:55], v16, s[24:27], s13 offen nt
	buffer_load_dwordx4 v[56:59], v16, s[24:27], s19 offen nt
	buffer_load_dwordx4 v[60:63], v16, s[24:27], s22 offen nt
	buffer_load_dwordx4 v[64:67], v16, s[24:27], s33 offen nt
	buffer_load_dwordx4 v[36:39], v16, s[24:27], s40 offen nt
	buffer_load_dwordx4 v[40:43], v16, s[24:27], s41 offen nt
	buffer_load_dwordx4 v[44:47], v16, s[24:27], s42 offen nt
	buffer_load_dwordx4 v[48:51], v16, s[24:27], s43 offen nt
	buffer_load_dwordx4 v[20:23], v16, s[24:27], s46 offen nt
	buffer_load_dwordx4 v[24:27], v16, s[24:27], s47 offen nt
	buffer_load_dwordx4 v[28:31], v16, s[24:27], s50 offen nt
	buffer_load_dwordx4 v[32:35], v16, s[24:27], s51 offen nt
	buffer_load_dwordx4 v[4:7], v16, s[24:27], s74 offen nt
	buffer_load_dwordx4 v[8:11], v16, s[24:27], s75 offen nt
	buffer_load_dwordx4 v[12:15], v16, s[24:27], s76 offen nt
	s_nop 0
	buffer_load_dwordx4 v[16:19], v16, s[24:27], s77 offen nt
	v_mov_b32_e32 v138, v3
	v_mov_b32_e32 v139, v3
	v_mov_b32_e32 v140, v3
	v_mov_b32_e32 v141, v3
	s_add_u32 s16, s10, s16
	s_addc_u32 s17, s11, s17
	s_add_u32 s16, s16, s79
	v_or_b32_e32 v132, s18, v134
	s_addc_u32 s17, s17, 0
	v_lshl_add_u64 v[136:137], s[16:17], 0, v[2:3]
	s_mov_b64 s[16:17], 0x14c00000
	v_ashrrev_i32_e32 v133, 31, v132
	v_lshl_add_u64 v[136:137], v[136:137], 0, s[16:17]
	v_lshlrev_b64 v[142:143], 10, v[132:133]
	v_lshl_add_u64 v[142:143], v[136:137], 0, v[142:143]
	s_or_b32 s16, s18, 64
	s_or_b32 s17, s18, 0x60
	s_waitcnt vmcnt(31)
	v_mul_f32_e32 v68, 0x42800000, v68
	s_waitcnt vmcnt(30)
	v_mul_f32_e32 v88, 0x42800000, v88
	v_cvt_pk_fp8_f32 v138, v68, v88
	s_waitcnt vmcnt(29)
	v_mul_f32_e32 v68, 0x42800000, v104
	s_waitcnt vmcnt(28)
	v_mul_f32_e32 v88, 0x42800000, v116
	v_cvt_pk_fp8_f32 v139, v68, v88
	s_waitcnt vmcnt(27)
	v_mul_f32_e32 v68, 0x42800000, v72
	s_waitcnt vmcnt(26)
	v_mul_f32_e32 v72, 0x42800000, v80
	v_cvt_pk_fp8_f32 v140, v68, v72
	s_waitcnt vmcnt(25)
	v_mul_f32_e32 v68, 0x42800000, v76
	s_waitcnt vmcnt(24)
	v_mul_f32_e32 v72, 0x42800000, v96
	v_cvt_pk_fp8_f32 v141, v68, v72
	v_mul_f32_e32 v68, 0x42800000, v69
	v_mul_f32_e32 v69, 0x42800000, v89
	s_waitcnt vmcnt(23)
	v_mul_f32_e32 v100, 0x42800000, v100
	s_waitcnt vmcnt(22)
	v_mul_f32_e32 v112, 0x42800000, v112
	v_cvt_pk_fp8_f32 v138, v100, v112 op_sel:[0,0,1]
	v_mul_f32_e32 v72, 0x42800000, v101
	s_waitcnt vmcnt(21)
	v_mul_f32_e32 v80, 0x42800000, v84
	s_waitcnt vmcnt(20)
	v_mul_f32_e32 v84, 0x42800000, v92
	v_cvt_pk_fp8_f32 v140, v80, v84 op_sel:[0,0,1]
	s_waitcnt vmcnt(15)
	v_mul_f32_e32 v52, 0x42800000, v52
	v_mul_f32_e32 v100, 0x42800000, v124
	v_mul_f32_e32 v104, 0x42800000, v128
	v_mul_f32_e32 v76, 0x42800000, v108
	v_mul_f32_e32 v80, 0x42800000, v120
	v_cvt_pk_fp8_f32 v139, v100, v104 op_sel:[0,0,1]
	v_cvt_pk_fp8_f32 v141, v76, v80 op_sel:[0,0,1]
	v_mul_f32_e32 v76, 0x42800000, v113
	s_waitcnt vmcnt(14)
	v_mul_f32_e32 v56, 0x42800000, v56
	s_waitcnt vmcnt(11)
	v_mul_f32_e32 v36, 0x42800000, v36
	global_store_dwordx4 v[142:143], v[138:141], off nt
	s_waitcnt vmcnt(11)
	v_mul_f32_e32 v40, 0x42800000, v40
	s_waitcnt vmcnt(8)
	v_mul_f32_e32 v20, 0x42800000, v20
	v_mov_b32_e32 v138, v3
	v_cvt_pk_fp8_f32 v138, v68, v69
	v_mul_f32_e32 v68, 0x42800000, v105
	v_mul_f32_e32 v69, 0x42800000, v117
	v_mov_b32_e32 v139, v3
	v_cvt_pk_fp8_f32 v139, v68, v69
	v_mul_f32_e32 v68, 0x42800000, v73
	v_mul_f32_e32 v69, 0x42800000, v81
	v_mov_b32_e32 v140, v3
	v_cvt_pk_fp8_f32 v140, v68, v69
	v_mul_f32_e32 v68, 0x42800000, v77
	v_mul_f32_e32 v69, 0x42800000, v97
	v_mov_b32_e32 v141, v3
	v_cvt_pk_fp8_f32 v141, v68, v69
	v_cvt_pk_fp8_f32 v138, v72, v76 op_sel:[0,0,1]
	v_mul_f32_e32 v72, 0x42800000, v125
	v_mul_f32_e32 v76, 0x42800000, v129
	v_cvt_pk_fp8_f32 v139, v72, v76 op_sel:[0,0,1]
	v_mul_f32_e32 v72, 0x42800000, v85
	v_mul_f32_e32 v73, 0x42800000, v93
	v_cvt_pk_fp8_f32 v140, v72, v73 op_sel:[0,0,1]
	v_mul_f32_e32 v72, 0x42800000, v109
	v_mul_f32_e32 v73, 0x42800000, v121
	v_cvt_pk_fp8_f32 v141, v72, v73 op_sel:[0,0,1]
	v_or_b32_e32 v68, 1, v132
	v_ashrrev_i32_e32 v69, 31, v68
	v_lshlrev_b64 v[68:69], 10, v[68:69]
	v_lshl_add_u64 v[68:69], v[136:137], 0, v[68:69]
	global_store_dwordx4 v[68:69], v[138:141], off nt
	v_mul_f32_e32 v68, 0x42800000, v70
	v_mul_f32_e32 v69, 0x42800000, v90
	v_mov_b32_e32 v138, v3
	v_cvt_pk_fp8_f32 v138, v68, v69
	v_mul_f32_e32 v68, 0x42800000, v106
	v_mul_f32_e32 v69, 0x42800000, v118
	v_mov_b32_e32 v139, v3
	v_cvt_pk_fp8_f32 v139, v68, v69
	v_mul_f32_e32 v68, 0x42800000, v74
	v_mul_f32_e32 v69, 0x42800000, v82
	v_mov_b32_e32 v140, v3
	v_cvt_pk_fp8_f32 v140, v68, v69
	v_mul_f32_e32 v68, 0x42800000, v78
	v_mul_f32_e32 v69, 0x42800000, v98
	v_mov_b32_e32 v141, v3
	v_mul_f32_e32 v70, 0x42800000, v102
	v_mul_f32_e32 v72, 0x42800000, v114
	v_cvt_pk_fp8_f32 v141, v68, v69
	v_cvt_pk_fp8_f32 v138, v70, v72 op_sel:[0,0,1]
	v_mul_f32_e32 v70, 0x42800000, v126
	v_mul_f32_e32 v72, 0x42800000, v130
	v_cvt_pk_fp8_f32 v139, v70, v72 op_sel:[0,0,1]
	v_mul_f32_e32 v70, 0x42800000, v86
	v_mul_f32_e32 v72, 0x42800000, v94
	v_cvt_pk_fp8_f32 v140, v70, v72 op_sel:[0,0,1]
	v_mul_f32_e32 v70, 0x42800000, v110
	v_mul_f32_e32 v72, 0x42800000, v122
	v_cvt_pk_fp8_f32 v141, v70, v72 op_sel:[0,0,1]
	v_or_b32_e32 v68, 2, v132
	v_ashrrev_i32_e32 v69, 31, v68
	v_lshlrev_b64 v[68:69], 10, v[68:69]
	v_lshl_add_u64 v[68:69], v[136:137], 0, v[68:69]
	global_store_dwordx4 v[68:69], v[138:141], off nt
	v_mul_f32_e32 v69, 0x42800000, v71
	v_mul_f32_e32 v70, 0x42800000, v91
	v_mov_b32_e32 v68, v3
	v_cvt_pk_fp8_f32 v68, v69, v70
	v_mul_f32_e32 v71, 0x42800000, v103
	v_mul_f32_e32 v72, 0x42800000, v115
	v_mul_f32_e32 v70, 0x42800000, v107
	v_cvt_pk_fp8_f32 v68, v71, v72 op_sel:[0,0,1]
	v_mul_f32_e32 v71, 0x42800000, v119
	v_mov_b32_e32 v69, v3
	v_cvt_pk_fp8_f32 v69, v70, v71
	v_mul_f32_e32 v72, 0x42800000, v127
	v_mul_f32_e32 v73, 0x42800000, v131
	v_mul_f32_e32 v71, 0x42800000, v75
	v_cvt_pk_fp8_f32 v69, v72, v73 op_sel:[0,0,1]
	v_mul_f32_e32 v72, 0x42800000, v83
	v_mov_b32_e32 v70, v3
	v_cvt_pk_fp8_f32 v70, v71, v72
	v_mul_f32_e32 v73, 0x42800000, v87
	v_mul_f32_e32 v74, 0x42800000, v95
	v_mul_f32_e32 v72, 0x42800000, v79
	v_cvt_pk_fp8_f32 v70, v73, v74 op_sel:[0,0,1]
	v_mul_f32_e32 v73, 0x42800000, v99
	v_mov_b32_e32 v71, v3
	v_cvt_pk_fp8_f32 v71, v72, v73
	v_mul_f32_e32 v74, 0x42800000, v111
	v_mul_f32_e32 v75, 0x42800000, v123
	v_or_b32_e32 v72, 3, v132
	v_cvt_pk_fp8_f32 v71, v74, v75 op_sel:[0,0,1]
	v_ashrrev_i32_e32 v73, 31, v72
	v_lshlrev_b64 v[72:73], 10, v[72:73]
	v_lshl_add_u64 v[72:73], v[136:137], 0, v[72:73]
	global_store_dwordx4 v[72:73], v[68:71], off nt
	v_mov_b32_e32 v138, v3
	v_mov_b32_e32 v139, v3
	v_add_u32_e32 v68, s16, v135
	s_waitcnt vmcnt(10)
	v_mul_f32_e32 v24, 0x42800000, v24
	v_mov_b32_e32 v140, v3
	s_waitcnt vmcnt(7)
	v_mul_f32_e32 v4, 0x42800000, v4
	s_waitcnt vmcnt(6)
	v_mul_f32_e32 v8, 0x42800000, v8
	v_mov_b32_e32 v141, v3
	v_or_b32_e32 v68, v68, v134
	v_cvt_pk_fp8_f32 v138, v52, v56
	v_cvt_pk_fp8_f32 v139, v36, v40
	v_cvt_pk_fp8_f32 v140, v20, v24
	v_cvt_pk_fp8_f32 v141, v4, v8
	v_lshlrev_b32_e32 v80, 2, v68
	buffer_load_dwordx4 v[116:119], v80, s[24:27], s13 offen nt
	buffer_load_dwordx4 v[120:123], v80, s[24:27], s19 offen nt
	buffer_load_dwordx4 v[124:127], v80, s[24:27], s22 offen nt
	buffer_load_dwordx4 v[128:131], v80, s[24:27], s33 offen nt
	buffer_load_dwordx4 v[100:103], v80, s[24:27], s40 offen nt
	buffer_load_dwordx4 v[104:107], v80, s[24:27], s41 offen nt
	buffer_load_dwordx4 v[108:111], v80, s[24:27], s42 offen nt
	buffer_load_dwordx4 v[112:115], v80, s[24:27], s43 offen nt
	buffer_load_dwordx4 v[84:87], v80, s[24:27], s46 offen nt
	buffer_load_dwordx4 v[88:91], v80, s[24:27], s47 offen nt
	buffer_load_dwordx4 v[92:95], v80, s[24:27], s50 offen nt
	buffer_load_dwordx4 v[96:99], v80, s[24:27], s51 offen nt
	buffer_load_dwordx4 v[68:71], v80, s[24:27], s74 offen nt
	buffer_load_dwordx4 v[72:75], v80, s[24:27], s75 offen nt
	buffer_load_dwordx4 v[76:79], v80, s[24:27], s76 offen nt
	s_nop 0
	buffer_load_dwordx4 v[80:83], v80, s[24:27], s77 offen nt
	v_mul_f32_e32 v60, 0x42800000, v60
	v_mul_f32_e32 v64, 0x42800000, v64
	v_mul_f32_e32 v44, 0x42800000, v44
	v_mul_f32_e32 v48, 0x42800000, v48
	v_mul_f32_e32 v28, 0x42800000, v28
	v_mul_f32_e32 v32, 0x42800000, v32
	s_waitcnt vmcnt(21)
	v_mul_f32_e32 v12, 0x42800000, v12
	s_waitcnt vmcnt(20)
	v_mul_f32_e32 v16, 0x42800000, v16
	v_or_b32_e32 v132, s78, v134
	v_cvt_pk_fp8_f32 v138, v60, v64 op_sel:[0,0,1]
	v_cvt_pk_fp8_f32 v139, v44, v48 op_sel:[0,0,1]
	v_cvt_pk_fp8_f32 v140, v28, v32 op_sel:[0,0,1]
	v_cvt_pk_fp8_f32 v141, v12, v16 op_sel:[0,0,1]
	v_ashrrev_i32_e32 v133, 31, v132
	v_lshlrev_b64 v[142:143], 10, v[132:133]
	v_lshl_add_u64 v[142:143], v[136:137], 0, v[142:143]
	global_store_dwordx4 v[142:143], v[138:141], off nt
	v_mul_f32_e32 v4, 0x42800000, v53
	v_mul_f32_e32 v8, 0x42800000, v57
	v_mov_b32_e32 v138, v3
	v_cvt_pk_fp8_f32 v138, v4, v8
	v_mul_f32_e32 v4, 0x42800000, v37
	v_mul_f32_e32 v8, 0x42800000, v41
	v_mov_b32_e32 v139, v3
	v_cvt_pk_fp8_f32 v139, v4, v8
	v_mul_f32_e32 v4, 0x42800000, v21
	v_mul_f32_e32 v8, 0x42800000, v25
	v_mov_b32_e32 v140, v3
	v_cvt_pk_fp8_f32 v140, v4, v8
	v_mul_f32_e32 v4, 0x42800000, v5
	v_mul_f32_e32 v5, 0x42800000, v9
	v_mov_b32_e32 v141, v3
	v_cvt_pk_fp8_f32 v141, v4, v5
	v_mul_f32_e32 v12, 0x42800000, v61
	v_mul_f32_e32 v16, 0x42800000, v65
	v_cvt_pk_fp8_f32 v138, v12, v16 op_sel:[0,0,1]
	v_mul_f32_e32 v12, 0x42800000, v45
	v_mul_f32_e32 v16, 0x42800000, v49
	v_cvt_pk_fp8_f32 v139, v12, v16 op_sel:[0,0,1]
	v_mul_f32_e32 v12, 0x42800000, v29
	v_mul_f32_e32 v16, 0x42800000, v33
	v_mul_f32_e32 v8, 0x42800000, v13
	v_mul_f32_e32 v9, 0x42800000, v17
	v_cvt_pk_fp8_f32 v140, v12, v16 op_sel:[0,0,1]
	v_cvt_pk_fp8_f32 v141, v8, v9 op_sel:[0,0,1]
	v_or_b32_e32 v4, 1, v132
	v_ashrrev_i32_e32 v5, 31, v4
	v_lshlrev_b64 v[4:5], 10, v[4:5]
	v_lshl_add_u64 v[4:5], v[136:137], 0, v[4:5]
	global_store_dwordx4 v[4:5], v[138:141], off nt
	v_mul_f32_e32 v4, 0x42800000, v54
	v_mul_f32_e32 v5, 0x42800000, v58
	v_mov_b32_e32 v138, v3
	v_cvt_pk_fp8_f32 v138, v4, v5
	v_mul_f32_e32 v4, 0x42800000, v38
	v_mul_f32_e32 v5, 0x42800000, v42
	v_mov_b32_e32 v139, v3
	v_cvt_pk_fp8_f32 v139, v4, v5
	v_mul_f32_e32 v4, 0x42800000, v22
	v_mul_f32_e32 v5, 0x42800000, v26
	v_mov_b32_e32 v140, v3
	v_cvt_pk_fp8_f32 v140, v4, v5
	v_mul_f32_e32 v4, 0x42800000, v6
	v_mul_f32_e32 v5, 0x42800000, v10
	v_mov_b32_e32 v141, v3
	v_mul_f32_e32 v8, 0x42800000, v62
	v_mul_f32_e32 v9, 0x42800000, v66
	v_cvt_pk_fp8_f32 v141, v4, v5
	v_cvt_pk_fp8_f32 v138, v8, v9 op_sel:[0,0,1]
	v_mul_f32_e32 v8, 0x42800000, v46
	v_mul_f32_e32 v9, 0x42800000, v50
	v_cvt_pk_fp8_f32 v139, v8, v9 op_sel:[0,0,1]
	v_mul_f32_e32 v8, 0x42800000, v30
	v_mul_f32_e32 v9, 0x42800000, v34
	v_cvt_pk_fp8_f32 v140, v8, v9 op_sel:[0,0,1]
	v_mul_f32_e32 v6, 0x42800000, v14
	v_mul_f32_e32 v8, 0x42800000, v18
	v_cvt_pk_fp8_f32 v141, v6, v8 op_sel:[0,0,1]
	v_or_b32_e32 v4, 2, v132
	v_ashrrev_i32_e32 v5, 31, v4
	v_lshlrev_b64 v[4:5], 10, v[4:5]
	v_lshl_add_u64 v[4:5], v[136:137], 0, v[4:5]
	global_store_dwordx4 v[4:5], v[138:141], off nt
	v_mul_f32_e32 v5, 0x42800000, v55
	v_mul_f32_e32 v6, 0x42800000, v59
	v_mov_b32_e32 v4, v3
	v_cvt_pk_fp8_f32 v4, v5, v6
	v_mul_f32_e32 v8, 0x42800000, v63
	v_mul_f32_e32 v9, 0x42800000, v67
	v_mul_f32_e32 v6, 0x42800000, v39
	v_cvt_pk_fp8_f32 v4, v8, v9 op_sel:[0,0,1]
	v_mul_f32_e32 v8, 0x42800000, v43
	v_mov_b32_e32 v5, v3
	v_cvt_pk_fp8_f32 v5, v6, v8
	v_mul_f32_e32 v9, 0x42800000, v47
	v_mul_f32_e32 v10, 0x42800000, v51
	v_mul_f32_e32 v8, 0x42800000, v23
	v_cvt_pk_fp8_f32 v5, v9, v10 op_sel:[0,0,1]
	v_mul_f32_e32 v9, 0x42800000, v27
	v_mov_b32_e32 v6, v3
	v_cvt_pk_fp8_f32 v6, v8, v9
	v_mul_f32_e32 v8, 0x42800000, v7
	v_mul_f32_e32 v9, 0x42800000, v11
	v_mov_b32_e32 v7, v3
	v_cvt_pk_fp8_f32 v7, v8, v9
	v_mul_f32_e32 v10, 0x42800000, v31
	v_mul_f32_e32 v12, 0x42800000, v35
	v_cvt_pk_fp8_f32 v6, v10, v12 op_sel:[0,0,1]
	v_mul_f32_e32 v10, 0x42800000, v15
	v_mul_f32_e32 v11, 0x42800000, v19
	v_cvt_pk_fp8_f32 v7, v10, v11 op_sel:[0,0,1]
	v_or_b32_e32 v8, 3, v132
	v_ashrrev_i32_e32 v9, 31, v8
	v_lshlrev_b64 v[8:9], 10, v[8:9]
	v_lshl_add_u64 v[8:9], v[136:137], 0, v[8:9]
	global_store_dwordx4 v[8:9], v[4:7], off nt
	s_waitcnt vmcnt(19)
	v_mul_f32_e32 v116, 0x42800000, v116
	s_waitcnt vmcnt(18)
	v_mul_f32_e32 v120, 0x42800000, v120
	v_add_u32_e32 v4, s17, v135
	v_or_b32_e32 v4, v4, v134
	v_lshlrev_b32_e32 v16, 2, v4
	buffer_load_dwordx4 v[52:55], v16, s[24:27], s13 offen nt
	buffer_load_dwordx4 v[56:59], v16, s[24:27], s19 offen nt
	buffer_load_dwordx4 v[60:63], v16, s[24:27], s22 offen nt
	buffer_load_dwordx4 v[64:67], v16, s[24:27], s33 offen nt
	buffer_load_dwordx4 v[36:39], v16, s[24:27], s40 offen nt
	buffer_load_dwordx4 v[40:43], v16, s[24:27], s41 offen nt
	buffer_load_dwordx4 v[44:47], v16, s[24:27], s42 offen nt
	buffer_load_dwordx4 v[48:51], v16, s[24:27], s43 offen nt
	buffer_load_dwordx4 v[20:23], v16, s[24:27], s46 offen nt
	buffer_load_dwordx4 v[24:27], v16, s[24:27], s47 offen nt
	buffer_load_dwordx4 v[28:31], v16, s[24:27], s50 offen nt
	buffer_load_dwordx4 v[32:35], v16, s[24:27], s51 offen nt
	buffer_load_dwordx4 v[4:7], v16, s[24:27], s74 offen nt
	buffer_load_dwordx4 v[8:11], v16, s[24:27], s75 offen nt
	buffer_load_dwordx4 v[12:15], v16, s[24:27], s76 offen nt
	s_nop 0
	buffer_load_dwordx4 v[16:19], v16, s[24:27], s77 offen nt
	v_mov_b32_e32 v138, v3
	s_waitcnt vmcnt(31)
	v_mul_f32_e32 v100, 0x42800000, v100
	s_waitcnt vmcnt(30)
	v_mul_f32_e32 v104, 0x42800000, v104
	v_mov_b32_e32 v139, v3
	s_waitcnt vmcnt(27)
	v_mul_f32_e32 v84, 0x42800000, v84
	s_waitcnt vmcnt(26)
	v_mul_f32_e32 v88, 0x42800000, v88
	v_mov_b32_e32 v140, v3
	s_waitcnt vmcnt(23)
	v_mul_f32_e32 v68, 0x42800000, v68
	s_waitcnt vmcnt(22)
	v_mul_f32_e32 v72, 0x42800000, v72
	v_mov_b32_e32 v141, v3
	v_cvt_pk_fp8_f32 v138, v116, v120
	v_cvt_pk_fp8_f32 v139, v100, v104
	v_cvt_pk_fp8_f32 v140, v84, v88
	v_cvt_pk_fp8_f32 v141, v68, v72
	v_mul_f32_e32 v124, 0x42800000, v124
	v_mul_f32_e32 v128, 0x42800000, v128
	v_mul_f32_e32 v108, 0x42800000, v108
	v_mul_f32_e32 v112, 0x42800000, v112
	v_mul_f32_e32 v92, 0x42800000, v92
	v_mul_f32_e32 v96, 0x42800000, v96
	s_waitcnt vmcnt(21)
	v_mul_f32_e32 v76, 0x42800000, v76
	s_waitcnt vmcnt(20)
	v_mul_f32_e32 v80, 0x42800000, v80
	v_or_b32_e32 v132, s16, v134
	v_cvt_pk_fp8_f32 v138, v124, v128 op_sel:[0,0,1]
	v_cvt_pk_fp8_f32 v139, v108, v112 op_sel:[0,0,1]
	v_cvt_pk_fp8_f32 v140, v92, v96 op_sel:[0,0,1]
	v_cvt_pk_fp8_f32 v141, v76, v80 op_sel:[0,0,1]
	v_ashrrev_i32_e32 v133, 31, v132
	v_lshlrev_b64 v[142:143], 10, v[132:133]
	v_lshl_add_u64 v[142:143], v[136:137], 0, v[142:143]
	global_store_dwordx4 v[142:143], v[138:141], off nt
	v_mul_f32_e32 v68, 0x42800000, v117
	v_mul_f32_e32 v72, 0x42800000, v121
	v_mov_b32_e32 v138, v3
	v_cvt_pk_fp8_f32 v138, v68, v72
	v_mul_f32_e32 v68, 0x42800000, v101
	v_mul_f32_e32 v72, 0x42800000, v105
	v_mov_b32_e32 v139, v3
	v_cvt_pk_fp8_f32 v139, v68, v72
	v_mul_f32_e32 v68, 0x42800000, v85
	v_mul_f32_e32 v72, 0x42800000, v89
	v_mov_b32_e32 v140, v3
	v_cvt_pk_fp8_f32 v140, v68, v72
	v_mul_f32_e32 v68, 0x42800000, v69
	v_mul_f32_e32 v69, 0x42800000, v73
	v_mov_b32_e32 v141, v3
	v_cvt_pk_fp8_f32 v141, v68, v69
	v_mul_f32_e32 v76, 0x42800000, v125
	v_mul_f32_e32 v80, 0x42800000, v129
	v_cvt_pk_fp8_f32 v138, v76, v80 op_sel:[0,0,1]
	v_mul_f32_e32 v76, 0x42800000, v109
	v_mul_f32_e32 v80, 0x42800000, v113
	v_cvt_pk_fp8_f32 v139, v76, v80 op_sel:[0,0,1]
	v_mul_f32_e32 v76, 0x42800000, v93
	v_mul_f32_e32 v80, 0x42800000, v97
	v_mul_f32_e32 v72, 0x42800000, v77
	v_mul_f32_e32 v73, 0x42800000, v81
	v_cvt_pk_fp8_f32 v140, v76, v80 op_sel:[0,0,1]
	v_cvt_pk_fp8_f32 v141, v72, v73 op_sel:[0,0,1]
	v_or_b32_e32 v68, 1, v132
	v_ashrrev_i32_e32 v69, 31, v68
	v_lshlrev_b64 v[68:69], 10, v[68:69]
	v_lshl_add_u64 v[68:69], v[136:137], 0, v[68:69]
	global_store_dwordx4 v[68:69], v[138:141], off nt
	v_mul_f32_e32 v68, 0x42800000, v118
	v_mul_f32_e32 v69, 0x42800000, v122
	v_mov_b32_e32 v138, v3
	v_cvt_pk_fp8_f32 v138, v68, v69
	v_mul_f32_e32 v68, 0x42800000, v102
	v_mul_f32_e32 v69, 0x42800000, v106
	v_mov_b32_e32 v139, v3
	v_cvt_pk_fp8_f32 v139, v68, v69
	v_mul_f32_e32 v68, 0x42800000, v86
	v_mul_f32_e32 v69, 0x42800000, v90
	v_mov_b32_e32 v140, v3
	v_cvt_pk_fp8_f32 v140, v68, v69
	v_mul_f32_e32 v68, 0x42800000, v70
	v_mul_f32_e32 v69, 0x42800000, v74
	v_mov_b32_e32 v141, v3
	v_mul_f32_e32 v72, 0x42800000, v126
	v_mul_f32_e32 v73, 0x42800000, v130
	v_cvt_pk_fp8_f32 v141, v68, v69
	v_cvt_pk_fp8_f32 v138, v72, v73 op_sel:[0,0,1]
	v_mul_f32_e32 v72, 0x42800000, v110
	v_mul_f32_e32 v73, 0x42800000, v114
	v_cvt_pk_fp8_f32 v139, v72, v73 op_sel:[0,0,1]
	v_mul_f32_e32 v72, 0x42800000, v94
	v_mul_f32_e32 v73, 0x42800000, v98
	v_cvt_pk_fp8_f32 v140, v72, v73 op_sel:[0,0,1]
	v_mul_f32_e32 v70, 0x42800000, v78
	v_mul_f32_e32 v72, 0x42800000, v82
	v_cvt_pk_fp8_f32 v141, v70, v72 op_sel:[0,0,1]
	v_or_b32_e32 v68, 2, v132
	v_ashrrev_i32_e32 v69, 31, v68
	v_lshlrev_b64 v[68:69], 10, v[68:69]
	v_lshl_add_u64 v[68:69], v[136:137], 0, v[68:69]
	global_store_dwordx4 v[68:69], v[138:141], off nt
	v_mul_f32_e32 v69, 0x42800000, v119
	v_mul_f32_e32 v70, 0x42800000, v123
	v_mov_b32_e32 v68, v3
	v_cvt_pk_fp8_f32 v68, v69, v70
	v_mul_f32_e32 v72, 0x42800000, v127
	v_mul_f32_e32 v73, 0x42800000, v131
	v_mul_f32_e32 v70, 0x42800000, v103
	v_cvt_pk_fp8_f32 v68, v72, v73 op_sel:[0,0,1]
	v_mul_f32_e32 v72, 0x42800000, v107
	v_mov_b32_e32 v69, v3
	v_cvt_pk_fp8_f32 v69, v70, v72
	v_mul_f32_e32 v73, 0x42800000, v111
	v_mul_f32_e32 v74, 0x42800000, v115
	v_mul_f32_e32 v72, 0x42800000, v87
	v_cvt_pk_fp8_f32 v69, v73, v74 op_sel:[0,0,1]
	v_mul_f32_e32 v73, 0x42800000, v91
	v_mov_b32_e32 v70, v3
	v_cvt_pk_fp8_f32 v70, v72, v73
	v_mul_f32_e32 v72, 0x42800000, v71
	v_mul_f32_e32 v73, 0x42800000, v75
	v_mov_b32_e32 v71, v3
	v_cvt_pk_fp8_f32 v71, v72, v73
	v_mul_f32_e32 v74, 0x42800000, v95
	v_mul_f32_e32 v76, 0x42800000, v99
	v_cvt_pk_fp8_f32 v70, v74, v76 op_sel:[0,0,1]
	v_mul_f32_e32 v74, 0x42800000, v79
	v_mul_f32_e32 v75, 0x42800000, v83
	v_cvt_pk_fp8_f32 v71, v74, v75 op_sel:[0,0,1]
	v_or_b32_e32 v72, 3, v132
	v_ashrrev_i32_e32 v73, 31, v72
	v_lshlrev_b64 v[72:73], 10, v[72:73]
	v_lshl_add_u64 v[72:73], v[136:137], 0, v[72:73]
	global_store_dwordx4 v[72:73], v[68:71], off nt
	s_waitcnt vmcnt(19)
	v_mul_f32_e32 v52, 0x42800000, v52
	s_waitcnt vmcnt(18)
	v_mul_f32_e32 v56, 0x42800000, v56
	v_mov_b32_e32 v70, v3
	s_waitcnt vmcnt(15)
	v_mul_f32_e32 v36, 0x42800000, v36
	s_waitcnt vmcnt(14)
	v_mul_f32_e32 v40, 0x42800000, v40
	v_mov_b32_e32 v71, v3
	s_waitcnt vmcnt(11)
	v_mul_f32_e32 v20, 0x42800000, v20
	s_waitcnt vmcnt(10)
	v_mul_f32_e32 v24, 0x42800000, v24
	v_mov_b32_e32 v72, v3
	s_waitcnt vmcnt(7)
	v_mul_f32_e32 v4, 0x42800000, v4
	s_waitcnt vmcnt(6)
	v_mul_f32_e32 v8, 0x42800000, v8
	v_mov_b32_e32 v73, v3
	v_cvt_pk_fp8_f32 v70, v52, v56
	v_cvt_pk_fp8_f32 v71, v36, v40
	v_cvt_pk_fp8_f32 v72, v20, v24
	v_cvt_pk_fp8_f32 v73, v4, v8
	v_mul_f32_e32 v60, 0x42800000, v60
	v_mul_f32_e32 v64, 0x42800000, v64
	v_mul_f32_e32 v44, 0x42800000, v44
	v_mul_f32_e32 v48, 0x42800000, v48
	v_mul_f32_e32 v28, 0x42800000, v28
	v_mul_f32_e32 v32, 0x42800000, v32
	s_waitcnt vmcnt(5)
	v_mul_f32_e32 v12, 0x42800000, v12
	s_waitcnt vmcnt(4)
	v_mul_f32_e32 v16, 0x42800000, v16
	v_or_b32_e32 v68, s17, v134
	v_cvt_pk_fp8_f32 v70, v60, v64 op_sel:[0,0,1]
	v_cvt_pk_fp8_f32 v71, v44, v48 op_sel:[0,0,1]
	v_cvt_pk_fp8_f32 v72, v28, v32 op_sel:[0,0,1]
	v_cvt_pk_fp8_f32 v73, v12, v16 op_sel:[0,0,1]
	v_ashrrev_i32_e32 v69, 31, v68
	v_lshlrev_b64 v[74:75], 10, v[68:69]
	v_lshl_add_u64 v[74:75], v[136:137], 0, v[74:75]
	global_store_dwordx4 v[74:75], v[70:73], off nt
	v_mul_f32_e32 v4, 0x42800000, v53
	v_mul_f32_e32 v8, 0x42800000, v57
	v_mov_b32_e32 v70, v3
	v_cvt_pk_fp8_f32 v70, v4, v8
	v_mul_f32_e32 v4, 0x42800000, v37
	v_mul_f32_e32 v8, 0x42800000, v41
	v_mov_b32_e32 v71, v3
	v_cvt_pk_fp8_f32 v71, v4, v8
	v_mul_f32_e32 v4, 0x42800000, v21
	v_mul_f32_e32 v8, 0x42800000, v25
	v_mov_b32_e32 v72, v3
	v_cvt_pk_fp8_f32 v72, v4, v8
	v_mul_f32_e32 v4, 0x42800000, v5
	v_mul_f32_e32 v5, 0x42800000, v9
	v_mov_b32_e32 v73, v3
	v_cvt_pk_fp8_f32 v73, v4, v5
	v_mul_f32_e32 v12, 0x42800000, v61
	v_mul_f32_e32 v16, 0x42800000, v65
	v_cvt_pk_fp8_f32 v70, v12, v16 op_sel:[0,0,1]
	v_mul_f32_e32 v12, 0x42800000, v45
	v_mul_f32_e32 v16, 0x42800000, v49
	v_cvt_pk_fp8_f32 v71, v12, v16 op_sel:[0,0,1]
	v_mul_f32_e32 v12, 0x42800000, v29
	v_mul_f32_e32 v16, 0x42800000, v33
	v_mul_f32_e32 v8, 0x42800000, v13
	v_mul_f32_e32 v9, 0x42800000, v17
	v_cvt_pk_fp8_f32 v72, v12, v16 op_sel:[0,0,1]
	v_cvt_pk_fp8_f32 v73, v8, v9 op_sel:[0,0,1]
	v_or_b32_e32 v4, 1, v68
	v_ashrrev_i32_e32 v5, 31, v4
	v_lshlrev_b64 v[4:5], 10, v[4:5]
	v_lshl_add_u64 v[4:5], v[136:137], 0, v[4:5]
	global_store_dwordx4 v[4:5], v[70:73], off nt
	v_mul_f32_e32 v4, 0x42800000, v54
	v_mul_f32_e32 v5, 0x42800000, v58
	v_mov_b32_e32 v70, v3
	v_cvt_pk_fp8_f32 v70, v4, v5
	v_mul_f32_e32 v4, 0x42800000, v38
	v_mul_f32_e32 v5, 0x42800000, v42
	v_mov_b32_e32 v71, v3
	v_cvt_pk_fp8_f32 v71, v4, v5
	v_mul_f32_e32 v4, 0x42800000, v22
	v_mul_f32_e32 v5, 0x42800000, v26
	v_mov_b32_e32 v72, v3
	v_cvt_pk_fp8_f32 v72, v4, v5
	v_mul_f32_e32 v4, 0x42800000, v6
	v_mul_f32_e32 v5, 0x42800000, v10
	v_mov_b32_e32 v73, v3
	v_mul_f32_e32 v8, 0x42800000, v62
	v_mul_f32_e32 v9, 0x42800000, v66
	v_cvt_pk_fp8_f32 v73, v4, v5
	v_cvt_pk_fp8_f32 v70, v8, v9 op_sel:[0,0,1]
	v_mul_f32_e32 v8, 0x42800000, v46
	v_mul_f32_e32 v9, 0x42800000, v50
	v_cvt_pk_fp8_f32 v71, v8, v9 op_sel:[0,0,1]
	v_mul_f32_e32 v8, 0x42800000, v30
	v_mul_f32_e32 v9, 0x42800000, v34
	v_cvt_pk_fp8_f32 v72, v8, v9 op_sel:[0,0,1]
	v_mul_f32_e32 v6, 0x42800000, v14
	v_mul_f32_e32 v8, 0x42800000, v18
	v_cvt_pk_fp8_f32 v73, v6, v8 op_sel:[0,0,1]
	v_or_b32_e32 v4, 2, v68
	v_ashrrev_i32_e32 v5, 31, v4
	v_lshlrev_b64 v[4:5], 10, v[4:5]
	v_lshl_add_u64 v[4:5], v[136:137], 0, v[4:5]
	global_store_dwordx4 v[4:5], v[70:73], off nt
	v_mul_f32_e32 v5, 0x42800000, v55
	v_mul_f32_e32 v6, 0x42800000, v59
	v_mov_b32_e32 v4, v3
	v_cvt_pk_fp8_f32 v4, v5, v6
	v_mul_f32_e32 v8, 0x42800000, v63
	v_mul_f32_e32 v9, 0x42800000, v67
	v_mul_f32_e32 v6, 0x42800000, v39
	v_cvt_pk_fp8_f32 v4, v8, v9 op_sel:[0,0,1]
	v_mul_f32_e32 v8, 0x42800000, v43
	v_mov_b32_e32 v5, v3
	v_cvt_pk_fp8_f32 v5, v6, v8
	v_mul_f32_e32 v9, 0x42800000, v47
	v_mul_f32_e32 v10, 0x42800000, v51
	v_mul_f32_e32 v8, 0x42800000, v23
	v_cvt_pk_fp8_f32 v5, v9, v10 op_sel:[0,0,1]
	v_mul_f32_e32 v9, 0x42800000, v27
	v_mov_b32_e32 v6, v3
	v_cvt_pk_fp8_f32 v6, v8, v9
	v_mul_f32_e32 v8, 0x42800000, v7
	v_mul_f32_e32 v9, 0x42800000, v11
	v_mov_b32_e32 v7, v3
	v_cvt_pk_fp8_f32 v7, v8, v9
	v_mul_f32_e32 v10, 0x42800000, v31
	v_mul_f32_e32 v12, 0x42800000, v35
	v_cvt_pk_fp8_f32 v6, v10, v12 op_sel:[0,0,1]
	v_mul_f32_e32 v10, 0x42800000, v15
	v_mul_f32_e32 v11, 0x42800000, v19
	v_cvt_pk_fp8_f32 v7, v10, v11 op_sel:[0,0,1]
	v_or_b32_e32 v8, 3, v68
	s_mov_b64 s[16:17], 0

.LBB0_975:
	s_getreg_b32 s100, hwreg(HW_REG_XCC_ID, 0, 4)
	s_and_b32 s100, s100, 7
	s_lshl_b32 s100, s100, 6
	v_mov_b32_e32 v252, s100
	s_and_saveexec_b64 s[100:101], s[0:1]
	s_cbranch_execz .Lap_skip
	v_mov_b32_e32 v253, 1
	s_nop 0
	global_atomic_add v251, v252, v253, s[30:31] sc0
.Lap_skip:
	s_or_b64 exec, exec, s[100:101]
	s_mov_b32 s98, 1
	v_add_u32_e32 v2, s40, v229
	ds_read_b64_tr_b16 v[194:195], v2 offset:24576
	ds_read_b64_tr_b16 v[196:197], v2 offset:25088
	v_add_f32_e32 v4, v82, v83
	v_add_f32_e32 v4, v84, v4
	v_add_f32_e32 v4, v85, v4
	v_add_f32_e32 v4, v86, v4
	v_add_f32_e32 v4, v87, v4
	v_cvt_pk_bf16_f32 v154, v82, v83
	v_cvt_pk_bf16_f32 v155, v84, v85
	s_waitcnt lgkmcnt(9)
	v_mfma_f32_32x32x16_bf16 v[98:113], v[190:193], v[158:161], v[50:65]
	ds_read_b64_tr_b16 v[126:127], v2 offset:28672
	ds_read_b64_tr_b16 v[128:129], v2 offset:29184
	s_waitcnt lgkmcnt(10)
	v_mfma_f32_32x32x16_bf16 v[50:65], v[186:189], v[158:161], v[50:65]
	v_add_f32_e32 v4, v88, v4
	v_add_f32_e32 v4, v89, v4
	v_add_f32_e32 v4, v90, v4
	v_add_f32_e32 v4, v91, v4
	v_cvt_pk_bf16_f32 v156, v86, v87
	v_cvt_pk_bf16_f32 v157, v88, v89
	ds_read_b64_tr_b16 v[122:123], v2 offset:25600
	ds_read_b64_tr_b16 v[124:125], v2 offset:26112
	v_add_f32_e32 v4, v92, v4
	v_add_f32_e32 v4, v93, v4
	v_add_f32_e32 v4, v94, v4
	v_add_f32_e32 v4, v95, v4
	v_cvt_pk_bf16_f32 v146, v90, v91
	v_cvt_pk_bf16_f32 v147, v92, v93
	s_waitcnt lgkmcnt(11)
	v_mfma_f32_32x32x16_bf16 v[98:113], v[182:185], v[150:153], v[98:113]
	ds_read_b64_tr_b16 v[118:119], v2 offset:29696
	ds_read_b64_tr_b16 v[120:121], v2 offset:30208
	s_waitcnt lgkmcnt(12)
	v_mfma_f32_32x32x16_bf16 v[50:65], v[178:181], v[150:153], v[50:65]
	v_add_f32_e32 v4, v96, v4
	v_add_f32_e32 v4, v97, v4
	v_add_f32_e32 v4, v66, v4
	v_add_f32_e32 v4, v67, v4
	v_cvt_pk_bf16_f32 v148, v94, v95
	v_cvt_pk_bf16_f32 v149, v96, v97
	ds_read_b64_tr_b16 v[114:115], v2 offset:26624
	ds_read_b64_tr_b16 v[116:117], v2 offset:27136
	v_add_f32_e32 v4, v68, v4
	v_add_f32_e32 v4, v69, v4
	v_add_f32_e32 v4, v70, v4
	v_add_f32_e32 v4, v71, v4
	v_cvt_pk_bf16_f32 v134, v66, v67
	v_cvt_pk_bf16_f32 v135, v68, v69
	s_waitcnt lgkmcnt(13)
	v_mfma_f32_32x32x16_bf16 v[98:113], v[174:177], v[142:145], v[98:113]
	ds_read_b64_tr_b16 v[12:13], v2 offset:30720
	ds_read_b64_tr_b16 v[14:15], v2 offset:31232
	s_waitcnt lgkmcnt(14)
	v_mfma_f32_32x32x16_bf16 v[50:65], v[170:173], v[142:145], v[50:65]
	v_add_f32_e32 v4, v72, v4
	v_add_f32_e32 v4, v73, v4
	v_add_f32_e32 v4, v74, v4
	v_add_f32_e32 v4, v75, v4
	v_cvt_pk_bf16_f32 v136, v70, v71
	v_cvt_pk_bf16_f32 v137, v72, v73
	ds_read_b64_tr_b16 v[8:9], v2 offset:27648
	ds_read_b64_tr_b16 v[10:11], v2 offset:28160
	v_add_f32_e32 v4, v76, v4
	v_add_f32_e32 v4, v77, v4
	v_add_f32_e32 v4, v78, v4
	v_add_f32_e32 v16, v79, v4
	v_cvt_pk_bf16_f32 v130, v74, v75
	v_cvt_pk_bf16_f32 v131, v76, v77
	s_waitcnt lgkmcnt(14)
	v_mfma_f32_32x32x16_bf16 v[98:113], v[166:169], v[138:141], v[98:113]
	ds_read_b64_tr_b16 v[4:5], v2 offset:31744
	ds_read_b64_tr_b16 v[6:7], v2 offset:32256
	v_mfma_f32_32x32x16_bf16 v[50:65], v[162:165], v[138:141], v[50:65]
	v_add_f32_e32 v2, v80, v16
	v_add_f32_e32 v2, v81, v2
	v_add_f32_e32 v2, 0, v2
	v_cvt_pk_bf16_f32 v132, v78, v79
	v_cvt_pk_bf16_f32 v133, v80, v81
	s_cmpk_lt_u32 s75, 0x180
	s_cselect_b64 vcc, -1, 0
	s_nop 1
	v_cndmask_b32_e32 v67, v99, v239, vcc
	v_cndmask_b32_e32 v66, v98, v239, vcc
	v_max_f32_e32 v16, v67, v67
	v_max_f32_e32 v17, v66, v66
	v_cndmask_b32_e32 v52, v52, v239, vcc
	v_cndmask_b32_e32 v51, v51, v239, vcc
	v_cndmask_b32_e32 v50, v50, v239, vcc
	v_cndmask_b32_e32 v69, v101, v239, vcc
	v_cndmask_b32_e32 v68, v100, v239, vcc
	v_max_f32_e32 v16, v17, v16
	v_cndmask_b32_e32 v53, v53, v239, vcc
	v_cndmask_b32_e32 v73, v105, v239, vcc
	v_cndmask_b32_e32 v72, v104, v239, vcc
	v_cndmask_b32_e32 v70, v102, v239, vcc
	v_max3_f32 v17, v68, v69, v51
	v_max3_f32 v16, v16, v50, v52
	v_cndmask_b32_e32 v57, v57, v239, vcc
	v_cndmask_b32_e32 v56, v56, v239, vcc
	v_cndmask_b32_e32 v54, v54, v239, vcc
	v_cndmask_b32_e32 v71, v103, v239, vcc
	v_max3_f32 v16, v16, v53, v70
	v_max3_f32 v17, v17, v72, v73
	v_cndmask_b32_e32 v55, v55, v239, vcc
	v_cndmask_b32_e32 v77, v109, v239, vcc
	v_cndmask_b32_e32 v76, v108, v239, vcc
	v_cndmask_b32_e32 v74, v106, v239, vcc
	v_max3_f32 v16, v16, v71, v54
	v_max3_f32 v17, v17, v56, v57
	v_cndmask_b32_e32 v61, v61, v239, vcc
	v_cndmask_b32_e32 v60, v60, v239, vcc
	v_cndmask_b32_e32 v58, v58, v239, vcc
	v_cndmask_b32_e32 v75, v107, v239, vcc
	v_max3_f32 v16, v16, v55, v74
	v_max3_f32 v17, v17, v76, v77
	v_cndmask_b32_e32 v59, v59, v239, vcc
	v_cndmask_b32_e32 v81, v113, v239, vcc
	v_cndmask_b32_e32 v80, v112, v239, vcc
	v_cndmask_b32_e32 v78, v110, v239, vcc
	v_max3_f32 v16, v16, v75, v58
	v_max3_f32 v17, v17, v60, v61
	v_cndmask_b32_e32 v65, v65, v239, vcc
	v_cndmask_b32_e32 v64, v64, v239, vcc
	v_cndmask_b32_e32 v62, v62, v239, vcc
	v_cndmask_b32_e32 v79, v111, v239, vcc
	v_max3_f32 v16, v16, v59, v78
	v_max3_f32 v17, v17, v80, v81
	v_cndmask_b32_e32 v63, v63, v239, vcc
	v_max3_f32 v16, v16, v79, v62
	v_max3_f32 v17, v17, v64, v65
	v_max3_f32 v16, v16, v63, v17
	v_mov_b32_e32 v17, v16
	s_nop 1
	v_permlane32_swap_b32_e32 v16, v17
	v_max_f32_e32 v17, v17, v17
	v_max_f32_e32 v16, v16, v16
	v_max_f32_e32 v16, v16, v17
	v_cmp_lt_f32_e32 vcc, s90, v16
	s_cmp_lg_u64 vcc, 0
	v_add_f32_e32 v2, v211, v2
	s_cselect_b64 s[4:5], -1, 0
	s_cbranch_vccnz .LBB0_980

.Ltp_use:
	s_mov_b32 s99, 0
	s_barrier
	s_and_saveexec_b64 s[8:9], s[0:1]
	s_cbranch_execz .LBB0_882
	s_mov_b64 s[12:13], exec
	v_mbcnt_lo_u32_b32 v2, s12, 0
	v_mbcnt_hi_u32_b32 v2, s13, v2
	s_waitcnt vmcnt(16)
	v_mov_b32_e32 v4, v250
	s_nop 1
	s_branch .Ltp_join
.Lap_use:
	s_mov_b32 s98, 0
	s_barrier
	s_and_saveexec_b64 s[74:75], s[0:1]
	s_cbranch_execz .LBB0_904
	s_mov_b64 s[4:5], exec
	v_mbcnt_lo_u32_b32 v2, s4, 0
	s_getreg_b32 s3, hwreg(HW_REG_XCC_ID, 0, 4)
	v_mbcnt_hi_u32_b32 v2, s5, v2
	s_and_b32 s2, s3, 7
	s_waitcnt vmcnt(16)
	v_mov_b32_e32 v4, v251
	s_nop 1
	s_branch .Lap_join
